# even out-projection tile head: dropped the compiler's vmcnt(0) that drained the LDS-DMA prologue in front of the K loop
# baseline (speedup 1.0000x reference)
; template <class Epi, bool ALIGN_EPI, bool SP2>
; __device__ __forceinline__ void gemm_phase(LAS unsigned char* lds, LAS float* tab, const Gemm g, const StaticOrder& S, const Epi& E, int wave_s) {
;     ...
;         const char* nA = has_next ? (const char*)g.A + (size_t)nxt.pm * tstepA + (nxt.hs > 0 ? hstepA : 0) : cA; const char* nB = has_next ? (const char*)g.Bt + (size_t)nxt.pn * tstepB : cB;
;         const bool half = cur.hs >= 0;
;         for (int t = 0; t < nt; t += 2) {
;             const bool last = (t == nt - 2);
;             const char* a1 = cA + (size_t)(t + 1) * kstep;
;             const char* a2 = last ? nA : cA + (size_t)(t + 2) * kstep; const char* b2 = last ? nB : cB + (size_t)(t + 2) * kstep;
;             const char* a3 = a2 + kstep; const char* b3 = b2 + kstep;
;     ...
; #pragma unroll
;         for (int a = 0; a < 2; ++a)
; #pragma unroll
;             for (int b = 0; b < 2; ++b)
; #pragma unroll
;                 for (int m = 0; m < 4; ++m)
; #pragma unroll
;                     for (int n = 0; n < 2; ++n) acc[a][b][m][n] = AccV{};
;         cur = nxt; cA = nA; cB = nB; ++ui;
.LBB0_1858:
	s_ashr_i32 s25, s24, 31
	s_lshl_b64 s[0:1], s[24:25], 19
	s_add_u32 s26, s41, s0
	s_addc_u32 s27, s42, s1
	s_and_b64 s[0:1], s[6:7], exec
	s_cselect_b32 s0, s27, s35
	s_cselect_b32 s1, s26, s34
	s_ashr_i32 s23, s22, 31
	s_lshl_b64 s[2:3], s[22:23], 19
	s_add_u32 s28, s43, s2
	s_addc_u32 s29, s44, s3
	s_and_b64 s[2:3], s[6:7], exec
	s_cselect_b32 s2, s29, s37
	s_cselect_b32 s3, s28, s36
	s_add_u32 s34, s34, 0x40080
	s_addc_u32 s35, s35, 0
	s_add_u32 s9, s36, 0x100
	v_mov_b32_e32 v2, 0
	s_addc_u32 s23, s37, 0
	s_mov_b32 s25, -2
	v_mov_b32_e32 v3, v2
	v_mov_b32_e32 v4, v2
	v_mov_b32_e32 v5, v2
	v_mov_b32_e32 v6, v2
	v_mov_b32_e32 v7, v2
	v_mov_b32_e32 v8, v2
	v_mov_b32_e32 v9, v2
	v_mov_b32_e32 v18, v2
	v_mov_b32_e32 v19, v2
	v_mov_b32_e32 v20, v2
	v_mov_b32_e32 v21, v2
	v_mov_b32_e32 v22, v2
	v_mov_b32_e32 v23, v2
	v_mov_b32_e32 v24, v2
	v_mov_b32_e32 v25, v2
	v_mov_b32_e32 v34, v2
	v_mov_b32_e32 v35, v2
	v_mov_b32_e32 v36, v2
	v_mov_b32_e32 v37, v2
	v_mov_b32_e32 v38, v2
	v_mov_b32_e32 v39, v2
	v_mov_b32_e32 v40, v2
	v_mov_b32_e32 v41, v2
	v_mov_b32_e32 v50, v2
	v_mov_b32_e32 v51, v2
	v_mov_b32_e32 v52, v2
	v_mov_b32_e32 v53, v2
	v_mov_b32_e32 v54, v2
	v_mov_b32_e32 v55, v2
	v_mov_b32_e32 v56, v2
	v_mov_b32_e32 v57, v2
	v_mov_b32_e32 v10, v2
	v_mov_b32_e32 v11, v2
	v_mov_b32_e32 v12, v2
	v_mov_b32_e32 v13, v2
	v_mov_b32_e32 v14, v2
	v_mov_b32_e32 v15, v2
	v_mov_b32_e32 v16, v2
	v_mov_b32_e32 v17, v2
	v_mov_b32_e32 v26, v2
	v_mov_b32_e32 v27, v2
	v_mov_b32_e32 v28, v2
	v_mov_b32_e32 v29, v2
	v_mov_b32_e32 v30, v2
	v_mov_b32_e32 v31, v2
	v_mov_b32_e32 v32, v2
	v_mov_b32_e32 v33, v2
	v_mov_b32_e32 v42, v2
	v_mov_b32_e32 v43, v2
	v_mov_b32_e32 v44, v2
	v_mov_b32_e32 v45, v2
	v_mov_b32_e32 v46, v2
	v_mov_b32_e32 v47, v2
	v_mov_b32_e32 v48, v2
	v_mov_b32_e32 v49, v2
	v_mov_b32_e32 v58, v2
	v_mov_b32_e32 v59, v2
	v_mov_b32_e32 v60, v2
	v_mov_b32_e32 v61, v2
	v_mov_b32_e32 v62, v2
	v_mov_b32_e32 v63, v2
	v_mov_b32_e32 v64, v2
	v_mov_b32_e32 v65, v2
	v_mov_b32_e32 v70, v2
	v_mov_b32_e32 v71, v2
	v_mov_b32_e32 v72, v2
	v_mov_b32_e32 v73, v2
	v_mov_b32_e32 v74, v2
	v_mov_b32_e32 v75, v2
	v_mov_b32_e32 v76, v2
	v_mov_b32_e32 v77, v2
	v_mov_b32_e32 v94, v2
	v_mov_b32_e32 v95, v2
	v_mov_b32_e32 v96, v2
	v_mov_b32_e32 v97, v2
	v_mov_b32_e32 v98, v2
	v_mov_b32_e32 v99, v2
	v_mov_b32_e32 v100, v2
	v_mov_b32_e32 v101, v2
	v_mov_b32_e32 v118, v2
	v_mov_b32_e32 v119, v2
	v_mov_b32_e32 v120, v2
	v_mov_b32_e32 v121, v2
	v_mov_b32_e32 v126, v2
	v_mov_b32_e32 v127, v2
	v_mov_b32_e32 v128, v2
	v_mov_b32_e32 v129, v2
	v_mov_b32_e32 v146, v2
	v_mov_b32_e32 v147, v2
	v_mov_b32_e32 v148, v2
	v_mov_b32_e32 v149, v2
	v_mov_b32_e32 v150, v2
	v_mov_b32_e32 v151, v2
	v_mov_b32_e32 v152, v2
	v_mov_b32_e32 v153, v2
	v_mov_b32_e32 v82, v2
	v_mov_b32_e32 v83, v2
	v_mov_b32_e32 v84, v2
	v_mov_b32_e32 v85, v2
	v_mov_b32_e32 v86, v2
	v_mov_b32_e32 v87, v2
	v_mov_b32_e32 v88, v2
	v_mov_b32_e32 v89, v2
	v_mov_b32_e32 v106, v2
	v_mov_b32_e32 v107, v2
	v_mov_b32_e32 v108, v2
	v_mov_b32_e32 v109, v2
	v_mov_b32_e32 v110, v2
	v_mov_b32_e32 v111, v2
	v_mov_b32_e32 v112, v2
	v_mov_b32_e32 v113, v2
	v_mov_b32_e32 v130, v2
	v_mov_b32_e32 v131, v2
	v_mov_b32_e32 v132, v2
	v_mov_b32_e32 v133, v2
	v_mov_b32_e32 v134, v2
	v_mov_b32_e32 v135, v2
	v_mov_b32_e32 v136, v2
	v_mov_b32_e32 v137, v2
	v_mov_b32_e32 v158, v2
	v_mov_b32_e32 v159, v2
	v_mov_b32_e32 v160, v2
	v_mov_b32_e32 v161, v2
	v_mov_b32_e32 v162, v2
	v_mov_b32_e32 v163, v2
	v_mov_b32_e32 v164, v2
	v_mov_b32_e32 v165, v2
